# baseline (speedup 1.0000x reference)
.LBB2_3:
	s_lshl_b32 s63, s53, 1
	s_add_i32 s61, s63, 2
	s_sub_i32 s2, s61, s40
	s_lshl_b32 s60, s53, 7
	s_min_i32 s62, s33, s2
	s_cmp_eq_u32 s55, 0
	s_cselect_b32 s79, 0, s62
	s_cmp_lt_i32 s2, 1
	s_waitcnt vmcnt(0)
	s_barrier
	s_cbranch_scc1 .LBB2_21
	s_add_i32 s63, s63, s55
	v_lshl_or_b32 v11, s63, 6, v83
	v_add_u32_e32 v10, s60, v82
	v_or_b32_e32 v12, 2, v11
	v_cmp_gt_i32_e64 s[6:7], v12, v10
	v_or_b32_e32 v12, 3, v11
	v_cmp_gt_i32_e64 s[8:9], v12, v10
	v_or_b32_e32 v12, 16, v11
	v_cmp_gt_i32_e64 s[10:11], v12, v10
	v_or_b32_e32 v12, 17, v11
	v_cmp_gt_i32_e64 s[12:13], v12, v10
	v_or_b32_e32 v12, 18, v11
	v_cmp_gt_i32_e64 s[14:15], v12, v10
	v_or_b32_e32 v12, 19, v11
	v_cmp_gt_i32_e64 s[16:17], v12, v10
	v_or_b32_e32 v12, 32, v11
	v_cmp_gt_i32_e64 s[18:19], v12, v10
	v_or_b32_e32 v12, 33, v11
	v_cmp_gt_i32_e64 s[20:21], v12, v10
	v_or_b32_e32 v12, 34, v11
	v_cmp_gt_i32_e64 s[22:23], v12, v10
	v_or_b32_e32 v12, 35, v11
	v_cmp_gt_i32_e64 s[24:25], v12, v10
	v_or_b32_e32 v12, 48, v11
	s_sub_i32 s37, s56, s40
	v_cmp_gt_i32_e64 s[26:27], v12, v10
	v_or_b32_e32 v12, 49, v11
	s_min_i32 s37, s33, s37
	v_cmp_gt_i32_e64 s[2:3], v11, v10
	v_cmp_lt_i32_e64 s[4:5], v11, v10
	v_cmp_gt_i32_e64 s[28:29], v12, v10
	v_or_b32_e32 v12, 50, v11
	v_or_b32_e32 v11, 51, v11
	s_max_i32 s37, s37, 1
	s_lshl_b64 s[38:39], s[40:41], 13
	v_mov_b32_e32 v67, 0
	v_cmp_gt_i32_e64 s[30:31], v12, v10
	v_cmp_gt_i32_e64 s[34:35], v11, v10
	s_mov_b32 s64, 1
	s_sub_i32 s65, 0, s37
	s_add_i32 s66, s40, s57
	s_add_u32 s68, s70, s38
	s_addc_u32 s69, s71, s39
	s_add_u32 s74, s72, s38
	s_addc_u32 s75, s73, s39
	v_mov_b32_e32 v14, v51
	v_mov_b32_e32 v15, v51
	v_mov_b32_e32 v16, v51
	v_mov_b32_e32 v17, v51
	s_mov_b64 s[38:39], -1
	v_mov_b32_e32 v30, 0
	v_mov_b32_e32 v31, v67
	v_mov_b32_e32 v32, v67
	v_mov_b32_e32 v33, v67
	v_mov_b32_e32 v26, 0
	v_mov_b32_e32 v27, v67
	v_mov_b32_e32 v28, v67
	v_mov_b32_e32 v29, v67
	v_mov_b32_e32 v22, v67
	v_mov_b32_e32 v23, v67
	v_mov_b32_e32 v24, v67
	v_mov_b32_e32 v25, v67
	v_mov_b32_e32 v18, v67
	v_mov_b32_e32 v19, v67
	v_mov_b32_e32 v20, v67
	v_mov_b32_e32 v21, v67
	v_mov_b32_e32 v10, v67
	v_mov_b32_e32 v11, v67
	v_mov_b32_e32 v12, v67
	v_mov_b32_e32 v13, v67
	s_mov_b32 s37, 0
	s_mov_b32 s80, 0
	s_mov_b32 s81, 0
	s_mov_b32 s83, s55
	s_mov_b32 s48, s40
	v_mov_b32_e32 v114, v57
	v_mov_b32_e32 v115, v81
	v_mov_b32_e32 v120, v57
	v_mov_b32_e32 v121, v81
	s_cmp_gt_u32 s48, s63
	s_branch .Lattn_after_rdv
.LBB2_5:
	ds_read_b128 v[102:105], v120 offset:8192
	ds_read_b128 v[106:109], v120 offset:10240
	ds_read_b128 v[110:113], v120 offset:12288
	v_exp_f32_e32 v69, v46
	v_exp_f32_e32 v71, v47
	v_exp_f32_e32 v73, v48
	v_exp_f32_e32 v75, v49
	ds_read_b128 v[46:49], v120 offset:14336
	v_exp_f32_e32 v42, v42
	v_exp_f32_e32 v43, v43
	v_exp_f32_e32 v44, v44
	v_exp_f32_e32 v45, v45
	v_cvt_pk_f16_f32 v76, v69, v71
	v_cvt_pk_f16_f32 v77, v73, v75
	v_cvt_pk_f16_f32 v78, v42, v43
	v_cvt_pk_f16_f32 v79, v44, v45
	ds_read_b128 v[42:45], v121 offset:8192
	v_exp_f32_e32 v38, v38
	v_exp_f32_e32 v39, v39
	s_waitcnt lgkmcnt(4)
	v_mfma_f32_16x16x32_f16 v[26:29], v[102:105], v[76:79], v[26:29]
	v_exp_f32_e32 v40, v40
	v_exp_f32_e32 v41, v41
	s_waitcnt lgkmcnt(3)
	v_mfma_f32_16x16x32_f16 v[22:25], v[106:109], v[76:79], v[22:25]
	ds_read_b128 v[102:105], v121 offset:10240
	v_exp_f32_e32 v34, v34
	v_exp_f32_e32 v35, v35
	s_waitcnt lgkmcnt(3)
	v_mfma_f32_16x16x32_f16 v[18:21], v[110:113], v[76:79], v[18:21]
	ds_read_b128 v[106:109], v121 offset:12288
	v_exp_f32_e32 v36, v36
	v_exp_f32_e32 v37, v37
	s_waitcnt lgkmcnt(3)
	v_mfma_f32_16x16x32_f16 v[10:13], v[46:49], v[76:79], v[10:13]
	ds_read_b128 v[110:113], v121 offset:14336
	v_mfma_f32_16x16x32_f16 v[14:17], v[116:119], v[76:79], v[14:17]
	v_cvt_pk_f16_f32 v37, v36, v37
	v_cvt_pk_f16_f32 v36, v34, v35
	v_cvt_pk_f16_f32 v35, v40, v41
	v_cvt_pk_f16_f32 v34, v38, v39
	s_mov_b64 s[38:39], 0
	s_cmp_lg_u32 s83, 0
	s_cbranch_scc1 .Lattn_B_tail_pf
	s_waitcnt lgkmcnt(3)
	v_mfma_f32_16x16x32_f16 v[26:29], v[42:45], v[34:37], v[26:29]
	s_waitcnt lgkmcnt(2)
	v_mfma_f32_16x16x32_f16 v[22:25], v[102:105], v[34:37], v[22:25]
	s_waitcnt lgkmcnt(1)
	v_mfma_f32_16x16x32_f16 v[18:21], v[106:109], v[34:37], v[18:21]
	s_waitcnt lgkmcnt(0)
	v_mfma_f32_16x16x32_f16 v[10:13], v[110:113], v[34:37], v[10:13]
	v_mfma_f32_16x16x32_f16 v[14:17], v[116:119], v[34:37], v[14:17]
	s_cmp_eq_u32 s55, 0
	s_cbranch_scc1 .LBB2_6
	s_mov_b32 s80, 0
	s_cmp_eq_u32 s81, 0
	s_cbranch_scc1 .Lattn_A
	s_branch .Lattn_post

.Lattn_A_join:
	s_waitcnt lgkmcnt(0)
	v_mfma_f32_16x16x32_f16 v[46:49], v[42:45], v[2:5], v[34:37]
	s_nop 2
	ds_read_b128 v[34:37], v115 offset:4096
	v_mfma_f32_16x16x32_f16 v[42:45], v[110:113], v[2:5], v[38:41]
	ds_read_b128 v[110:113], v115 offset:6144
	s_waitcnt lgkmcnt(0)
	v_mfma_f32_16x16x32_f16 v[38:41], v[34:37], v[2:5], v[102:105]
	v_mfma_f32_16x16x32_f16 v[34:37], v[110:113], v[2:5], v[106:109]
	s_cbranch_scc1 .LBB2_12
	v_cndmask_b32_e64 v69, v46, v100, s[2:3]
	v_cndmask_b32_e64 v46, v69, v46, s[4:5]
	v_cndmask_b32_e64 v47, v100, v47, s[4:5]
	v_cndmask_b32_e64 v48, v48, v100, s[6:7]
	v_cndmask_b32_e64 v49, v49, v100, s[8:9]
	v_cndmask_b32_e64 v42, v42, v100, s[10:11]
	v_cndmask_b32_e64 v43, v43, v100, s[12:13]
	v_cndmask_b32_e64 v44, v44, v100, s[14:15]
	v_cndmask_b32_e64 v45, v45, v100, s[16:17]
	v_cndmask_b32_e64 v38, v38, v100, s[18:19]
	v_cndmask_b32_e64 v39, v39, v100, s[20:21]
	v_cndmask_b32_e64 v40, v40, v100, s[22:23]
	v_cndmask_b32_e64 v41, v41, v100, s[24:25]
	v_cndmask_b32_e64 v34, v34, v100, s[26:27]
	v_cndmask_b32_e64 v35, v35, v100, s[28:29]
	v_cndmask_b32_e64 v36, v36, v100, s[30:31]
	v_cndmask_b32_e64 v37, v37, v100, s[34:35]

.Lattn_B_tail_pf:
	ds_read_b128 v[76:79], v114
	ds_read_b128 v[38:41], v114 offset:2048
	ds_read_b128 v[46:49], v114 offset:6144
	s_waitcnt lgkmcnt(6)
	v_mfma_f32_16x16x32_f16 v[26:29], v[42:45], v[34:37], v[26:29]
	s_waitcnt lgkmcnt(5)
	v_mfma_f32_16x16x32_f16 v[22:25], v[102:105], v[34:37], v[22:25]
	s_waitcnt lgkmcnt(4)
	v_mfma_f32_16x16x32_f16 v[18:21], v[106:109], v[34:37], v[18:21]
	s_waitcnt lgkmcnt(3)
	v_mfma_f32_16x16x32_f16 v[10:13], v[110:113], v[34:37], v[10:13]
	v_mfma_f32_16x16x32_f16 v[14:17], v[116:119], v[34:37], v[14:17]
	s_mov_b32 s80, 0
	ds_read_b128 v[42:45], v114 offset:4096
	ds_read_b128 v[110:113], v115 offset:2048
	s_add_i32 s48, s66, s64
	s_cmp_lg_u32 s48, 1
	s_waitcnt lgkmcnt(4)
	v_mfma_f32_16x16x32_f16 v[34:37], v[76:79], v[6:9], v[30:33]
	s_waitcnt lgkmcnt(1)
	v_mfma_f32_16x16x32_f16 v[102:105], v[42:45], v[6:9], v[30:33]
	ds_read_b128 v[42:45], v115
	v_mfma_f32_16x16x32_f16 v[38:41], v[38:41], v[6:9], v[30:33]
	v_mfma_f32_16x16x32_f16 v[106:109], v[46:49], v[6:9], v[30:33]
	s_branch .Lattn_A_join

.Lattn_last_step:
	s_cmp_eq_u32 s80, 0
	s_cbranch_scc1 .Lattn_post
	v_mov_b32_e32 v120, v114
	v_mov_b32_e32 v121, v115
	s_mov_b32 s81, 1
	s_mov_b32 s83, 0
	s_branch .LBB2_5
